# merge GEMM mid-K gate rescale: all 32 gate loads issued up front into free fragment registers with counted waits (hipcc kept about 5 in flight)
# speedup vs baseline: 1.0054x; 1.0028x over previous
; template <class Epi, class Sched, bool ALIGN_EPI = false, bool SP2 = false, bool F8 = false, bool GATHER = false>
; __device__ __forceinline__ void gemm_phase(PG8_LAS unsigned char* lds, const Gemm g, const Sched& S, const Epi& E) {
;     ...
;             if constexpr (Epi::CHAIN) { if (t == Epi::MID_T) {
;                 if constexpr (F8) asm volatile("s_nop 15\n\ts_nop 15" ::: "memory");
;                 int fr_ = fr, fq_ = fq; asm volatile("" : "+v"(fr_), "+v"(fq_)); E.mid(acc, cur, wr, wc, fr_, fq_); } }
;     __device__ __forceinline__ void mid(f32x4 (&acc)[2][2][4][2], const Unit& u, int wr, int wc, int fr, int fq) const {
;         int row0 = u.pm * 256 + wr * 64 + fr, col0 = u.pn * 256 + wc * 32 + 8 * fq; asm volatile("" : "+v"(row0), "+v"(col0));
; #pragma unroll
;         for (int ai = 0; ai < 2; ++ai)
; #pragma unroll
;             for (int m = 0; m < 4; ++m) { const size_t row = (size_t)(row0 + ai * 128 + m * 16);
; #pragma unroll
;                 for (int bj = 0; bj < 2; ++bj) { const int col = col0 + bj * 128; const v2u ga = *(const v2u*)(GATES + row * 4096 + col), gs = *(const v2u*)(GATES + row * 4096 + 2048 + col);
;                     f32x4& a0 = acc[ai][bj][m][0]; f32x4& a1 = acc[ai][bj][m][1];
; #pragma unroll
;                     for (int e = 0; e < 4; ++e) { a0[e] *= (float)((ga.x >> (8 * e)) & 0xffu) * __builtin_amdgcn_rcpf((float)((gs.x >> (8 * e)) & 0xffu));
;                                                   a1[e] *= (float)((ga.y >> (8 * e)) & 0xffu) * __builtin_amdgcn_rcpf((float)((gs.y >> (8 * e)) & 0xffu)); } } }
.LBB0_955:
	s_cmpk_lg_i32 s40, 0x400
	s_cbranch_scc1 .LBB0_954
	v_mov_b32_e32 v2, v1
	v_mov_b32_e32 v3, v179
	s_nop 15
	s_nop 15
	s_mov_b64 s[42:43], 0x10000
	v_add_u32_e32 v2, s29, v2
	v_lshl_add_u32 v4, v3, 3, s69
	s_nop 0
	v_ashrrev_i32_e32 v3, 31, v2
	v_lshlrev_b64 v[2:3], 12, v[2:3]
	v_lshl_add_u64 v[2:3], s[6:7], 0, v[2:3]
	v_ashrrev_i32_e32 v5, 31, v4
	v_lshl_add_u64 v[2:3], v[2:3], 0, v[4:5]
	global_load_dwordx2 v[8:9], v[2:3], off
	global_load_dwordx2 v[10:11], v[2:3], off offset:128
	global_load_dwordx2 v[12:13], v[2:3], off offset:2048
	global_load_dwordx2 v[14:15], v[2:3], off offset:2176
	v_lshl_add_u64 v[6:7], v[2:3], 0, s[42:43]
	global_load_dwordx2 v[16:17], v[6:7], off
	global_load_dwordx2 v[18:19], v[6:7], off offset:128
	global_load_dwordx2 v[20:21], v[6:7], off offset:2048
	global_load_dwordx2 v[22:23], v[6:7], off offset:2176
	v_lshl_add_u64 v[4:5], v[2:3], 0, s[14:15]
	global_load_dwordx2 v[24:25], v[4:5], off
	global_load_dwordx2 v[28:29], v[4:5], off offset:128
	global_load_dwordx2 v[180:181], v[4:5], off offset:2048
	global_load_dwordx2 v[182:183], v[4:5], off offset:2176
	v_lshl_add_u64 v[6:7], v[2:3], 0, s[16:17]
	global_load_dwordx2 v[184:185], v[6:7], off
	global_load_dwordx2 v[190:191], v[6:7], off offset:128
	global_load_dwordx2 v[192:193], v[6:7], off offset:2048
	global_load_dwordx2 v[194:195], v[6:7], off offset:2176
	v_lshl_add_u64 v[4:5], v[2:3], 0, s[18:19]
	global_load_dwordx2 v[196:197], v[4:5], off
	global_load_dwordx2 v[198:199], v[4:5], off offset:128
	global_load_dwordx2 v[200:201], v[4:5], off offset:2048
	global_load_dwordx2 v[202:203], v[4:5], off offset:2176
	v_lshl_add_u64 v[6:7], v[2:3], 0, s[20:21]
	global_load_dwordx2 v[204:205], v[6:7], off
	global_load_dwordx2 v[206:207], v[6:7], off offset:128
	global_load_dwordx2 v[208:209], v[6:7], off offset:2048
	global_load_dwordx2 v[210:211], v[6:7], off offset:2176
	v_lshl_add_u64 v[4:5], v[2:3], 0, s[22:23]
	global_load_dwordx2 v[212:213], v[4:5], off
	global_load_dwordx2 v[214:215], v[4:5], off offset:128
	global_load_dwordx2 v[216:217], v[4:5], off offset:2048
	global_load_dwordx2 v[218:219], v[4:5], off offset:2176
	v_lshl_add_u64 v[6:7], v[2:3], 0, s[24:25]
	global_load_dwordx2 v[220:221], v[6:7], off
	global_load_dwordx2 v[222:223], v[6:7], off offset:128
	global_load_dwordx2 v[224:225], v[6:7], off offset:2048
	global_load_dwordx2 v[226:227], v[6:7], off offset:2176
	s_waitcnt vmcnt(28)
	v_cvt_f32_ubyte0_e32 v232, v15
	v_cvt_f32_ubyte1_e32 v233, v15
	v_rcp_iflag_f32_e32 v232, v232
	v_rcp_iflag_f32_e32 v233, v233
	v_cvt_f32_ubyte0_e32 v234, v11
	v_cvt_f32_ubyte1_e32 v235, v11
	v_pk_mul_f32 v[232:233], v[232:233], v[234:235]
	v_pk_mul_f32 v[142:143], v[142:143], v[232:233]
	v_cvt_f32_ubyte2_e32 v236, v15
	v_cvt_f32_ubyte3_e32 v237, v15
	v_rcp_iflag_f32_e32 v236, v236
	v_rcp_iflag_f32_e32 v237, v237
	v_cvt_f32_ubyte2_e32 v238, v11
	v_cvt_f32_ubyte3_e32 v239, v11
	v_pk_mul_f32 v[236:237], v[236:237], v[238:239]
	v_pk_mul_f32 v[144:145], v[144:145], v[236:237]
	v_cvt_f32_ubyte0_e32 v232, v14
	v_cvt_f32_ubyte1_e32 v233, v14
	v_rcp_iflag_f32_e32 v232, v232
	v_rcp_iflag_f32_e32 v233, v233
	v_cvt_f32_ubyte0_e32 v234, v10
	v_cvt_f32_ubyte1_e32 v235, v10
	v_pk_mul_f32 v[232:233], v[232:233], v[234:235]
	v_pk_mul_f32 v[146:147], v[146:147], v[232:233]
	v_cvt_f32_ubyte2_e32 v236, v14
	v_cvt_f32_ubyte3_e32 v237, v14
	v_rcp_iflag_f32_e32 v236, v236
	v_rcp_iflag_f32_e32 v237, v237
	v_cvt_f32_ubyte2_e32 v238, v10
	v_cvt_f32_ubyte3_e32 v239, v10
	v_pk_mul_f32 v[236:237], v[236:237], v[238:239]
	v_pk_mul_f32 v[148:149], v[148:149], v[236:237]
	v_cvt_f32_ubyte0_e32 v232, v13
	v_cvt_f32_ubyte1_e32 v233, v13
	v_rcp_iflag_f32_e32 v232, v232
	v_rcp_iflag_f32_e32 v233, v233
	v_cvt_f32_ubyte0_e32 v234, v9
	v_cvt_f32_ubyte1_e32 v235, v9
	v_pk_mul_f32 v[232:233], v[232:233], v[234:235]
	v_pk_mul_f32 v[150:151], v[150:151], v[232:233]
	v_cvt_f32_ubyte2_e32 v236, v13
	v_cvt_f32_ubyte3_e32 v237, v13
	v_rcp_iflag_f32_e32 v236, v236
	v_rcp_iflag_f32_e32 v237, v237
	v_cvt_f32_ubyte2_e32 v238, v9
	v_cvt_f32_ubyte3_e32 v239, v9
	v_pk_mul_f32 v[236:237], v[236:237], v[238:239]
	v_pk_mul_f32 v[152:153], v[152:153], v[236:237]
	v_cvt_f32_ubyte0_e32 v232, v12
	v_cvt_f32_ubyte1_e32 v233, v12
	v_rcp_iflag_f32_e32 v232, v232
	v_rcp_iflag_f32_e32 v233, v233
	v_cvt_f32_ubyte0_e32 v234, v8
	v_cvt_f32_ubyte1_e32 v235, v8
	v_pk_mul_f32 v[232:233], v[232:233], v[234:235]
	v_pk_mul_f32 v[154:155], v[154:155], v[232:233]
	v_cvt_f32_ubyte2_e32 v236, v12
	v_cvt_f32_ubyte3_e32 v237, v12
	v_rcp_iflag_f32_e32 v236, v236
	v_rcp_iflag_f32_e32 v237, v237
	v_cvt_f32_ubyte2_e32 v238, v8
	v_cvt_f32_ubyte3_e32 v239, v8
	v_pk_mul_f32 v[236:237], v[236:237], v[238:239]
	v_pk_mul_f32 v[156:157], v[156:157], v[236:237]
	s_waitcnt vmcnt(24)
;     __device__ __forceinline__ void mid(f32x4 (&acc)[2][2][4][2], const Unit& u, int wr, int wc, int fr, int fq) const {
;     ...
;         for (int ai = 0; ai < 2; ++ai)
; #pragma unroll
;             for (int m = 0; m < 4; ++m) { const size_t row = (size_t)(row0 + ai * 128 + m * 16);
; #pragma unroll
;                 for (int bj = 0; bj < 2; ++bj) { const int col = col0 + bj * 128; const v2u ga = *(const v2u*)(GATES + row * 4096 + col), gs = *(const v2u*)(GATES + row * 4096 + 2048 + col);
;                     f32x4& a0 = acc[ai][bj][m][0]; f32x4& a1 = acc[ai][bj][m][1];
; #pragma unroll
;                     for (int e = 0; e < 4; ++e) { a0[e] *= (float)((ga.x >> (8 * e)) & 0xffu) * __builtin_amdgcn_rcpf((float)((gs.x >> (8 * e)) & 0xffu));
;                                                   a1[e] *= (float)((ga.y >> (8 * e)) & 0xffu) * __builtin_amdgcn_rcpf((float)((gs.y >> (8 * e)) & 0xffu)); } } }
	v_cvt_f32_ubyte0_e32 v232, v23
	v_cvt_f32_ubyte1_e32 v233, v23
	v_rcp_iflag_f32_e32 v232, v232
	v_rcp_iflag_f32_e32 v233, v233
	v_cvt_f32_ubyte0_e32 v234, v19
	v_cvt_f32_ubyte1_e32 v235, v19
	v_pk_mul_f32 v[232:233], v[232:233], v[234:235]
	v_pk_mul_f32 v[126:127], v[126:127], v[232:233]
	v_cvt_f32_ubyte2_e32 v236, v23
	v_cvt_f32_ubyte3_e32 v237, v23
	v_rcp_iflag_f32_e32 v236, v236
	v_rcp_iflag_f32_e32 v237, v237
	v_cvt_f32_ubyte2_e32 v238, v19
	v_cvt_f32_ubyte3_e32 v239, v19
	v_pk_mul_f32 v[236:237], v[236:237], v[238:239]
	v_pk_mul_f32 v[128:129], v[128:129], v[236:237]
	v_cvt_f32_ubyte0_e32 v232, v22
	v_cvt_f32_ubyte1_e32 v233, v22
	v_rcp_iflag_f32_e32 v232, v232
	v_rcp_iflag_f32_e32 v233, v233
	v_cvt_f32_ubyte0_e32 v234, v18
	v_cvt_f32_ubyte1_e32 v235, v18
	v_pk_mul_f32 v[232:233], v[232:233], v[234:235]
	v_pk_mul_f32 v[130:131], v[130:131], v[232:233]
	v_cvt_f32_ubyte2_e32 v236, v22
	v_cvt_f32_ubyte3_e32 v237, v22
	v_rcp_iflag_f32_e32 v236, v236
	v_rcp_iflag_f32_e32 v237, v237
	v_cvt_f32_ubyte2_e32 v238, v18
	v_cvt_f32_ubyte3_e32 v239, v18
	v_pk_mul_f32 v[236:237], v[236:237], v[238:239]
	v_pk_mul_f32 v[132:133], v[132:133], v[236:237]
	v_cvt_f32_ubyte0_e32 v232, v21
	v_cvt_f32_ubyte1_e32 v233, v21
	v_rcp_iflag_f32_e32 v232, v232
	v_rcp_iflag_f32_e32 v233, v233
	v_cvt_f32_ubyte0_e32 v234, v17
	v_cvt_f32_ubyte1_e32 v235, v17
	v_pk_mul_f32 v[232:233], v[232:233], v[234:235]
	v_pk_mul_f32 v[134:135], v[134:135], v[232:233]
	v_cvt_f32_ubyte2_e32 v236, v21
	v_cvt_f32_ubyte3_e32 v237, v21
	v_rcp_iflag_f32_e32 v236, v236
	v_rcp_iflag_f32_e32 v237, v237
	v_cvt_f32_ubyte2_e32 v238, v17
	v_cvt_f32_ubyte3_e32 v239, v17
	v_pk_mul_f32 v[236:237], v[236:237], v[238:239]
	v_pk_mul_f32 v[136:137], v[136:137], v[236:237]
	v_cvt_f32_ubyte0_e32 v232, v20
	v_cvt_f32_ubyte1_e32 v233, v20
	v_rcp_iflag_f32_e32 v232, v232
	v_rcp_iflag_f32_e32 v233, v233
	v_cvt_f32_ubyte0_e32 v234, v16
	v_cvt_f32_ubyte1_e32 v235, v16
	v_pk_mul_f32 v[232:233], v[232:233], v[234:235]
	v_pk_mul_f32 v[138:139], v[138:139], v[232:233]
	v_cvt_f32_ubyte2_e32 v236, v20
	v_cvt_f32_ubyte3_e32 v237, v20
	v_rcp_iflag_f32_e32 v236, v236
	v_rcp_iflag_f32_e32 v237, v237
	v_cvt_f32_ubyte2_e32 v238, v16
	v_cvt_f32_ubyte3_e32 v239, v16
	v_pk_mul_f32 v[236:237], v[236:237], v[238:239]
	v_pk_mul_f32 v[140:141], v[140:141], v[236:237]
	s_waitcnt vmcnt(20)
	v_cvt_f32_ubyte0_e32 v232, v183
	v_cvt_f32_ubyte1_e32 v233, v183
	v_rcp_iflag_f32_e32 v232, v232
	v_rcp_iflag_f32_e32 v233, v233
	v_cvt_f32_ubyte0_e32 v234, v29
	v_cvt_f32_ubyte1_e32 v235, v29
	v_pk_mul_f32 v[232:233], v[232:233], v[234:235]
	v_pk_mul_f32 v[110:111], v[110:111], v[232:233]
	v_cvt_f32_ubyte2_e32 v236, v183
	v_cvt_f32_ubyte3_e32 v237, v183
	v_rcp_iflag_f32_e32 v236, v236
	v_rcp_iflag_f32_e32 v237, v237
	v_cvt_f32_ubyte2_e32 v238, v29
	v_cvt_f32_ubyte3_e32 v239, v29
	v_pk_mul_f32 v[236:237], v[236:237], v[238:239]
	v_pk_mul_f32 v[112:113], v[112:113], v[236:237]
	v_cvt_f32_ubyte0_e32 v232, v182
	v_cvt_f32_ubyte1_e32 v233, v182
	v_rcp_iflag_f32_e32 v232, v232
	v_rcp_iflag_f32_e32 v233, v233
	v_cvt_f32_ubyte0_e32 v234, v28
	v_cvt_f32_ubyte1_e32 v235, v28
	v_pk_mul_f32 v[232:233], v[232:233], v[234:235]
	v_pk_mul_f32 v[114:115], v[114:115], v[232:233]
	v_cvt_f32_ubyte2_e32 v236, v182
	v_cvt_f32_ubyte3_e32 v237, v182
	v_rcp_iflag_f32_e32 v236, v236
	v_rcp_iflag_f32_e32 v237, v237
	v_cvt_f32_ubyte2_e32 v238, v28
	v_cvt_f32_ubyte3_e32 v239, v28
	v_pk_mul_f32 v[236:237], v[236:237], v[238:239]
	v_pk_mul_f32 v[116:117], v[116:117], v[236:237]
	v_cvt_f32_ubyte0_e32 v232, v181
	v_cvt_f32_ubyte1_e32 v233, v181
	v_rcp_iflag_f32_e32 v232, v232
	v_rcp_iflag_f32_e32 v233, v233
	v_cvt_f32_ubyte0_e32 v234, v25
	v_cvt_f32_ubyte1_e32 v235, v25
	v_pk_mul_f32 v[232:233], v[232:233], v[234:235]
	v_pk_mul_f32 v[118:119], v[118:119], v[232:233]
	v_cvt_f32_ubyte2_e32 v236, v181
	v_cvt_f32_ubyte3_e32 v237, v181
	v_rcp_iflag_f32_e32 v236, v236
	v_rcp_iflag_f32_e32 v237, v237
	v_cvt_f32_ubyte2_e32 v238, v25
	v_cvt_f32_ubyte3_e32 v239, v25
	v_pk_mul_f32 v[236:237], v[236:237], v[238:239]
	v_pk_mul_f32 v[120:121], v[120:121], v[236:237]
	v_cvt_f32_ubyte0_e32 v232, v180
	v_cvt_f32_ubyte1_e32 v233, v180
	v_rcp_iflag_f32_e32 v232, v232
	v_rcp_iflag_f32_e32 v233, v233
	v_cvt_f32_ubyte0_e32 v234, v24
	v_cvt_f32_ubyte1_e32 v235, v24
	v_pk_mul_f32 v[232:233], v[232:233], v[234:235]
	v_pk_mul_f32 v[122:123], v[122:123], v[232:233]
	v_cvt_f32_ubyte2_e32 v236, v180
	v_cvt_f32_ubyte3_e32 v237, v180
	v_rcp_iflag_f32_e32 v236, v236
	v_rcp_iflag_f32_e32 v237, v237
	v_cvt_f32_ubyte2_e32 v238, v24
	v_cvt_f32_ubyte3_e32 v239, v24
	v_pk_mul_f32 v[236:237], v[236:237], v[238:239]
	v_pk_mul_f32 v[124:125], v[124:125], v[236:237]
	s_waitcnt vmcnt(16)
;     __device__ __forceinline__ void mid(f32x4 (&acc)[2][2][4][2], const Unit& u, int wr, int wc, int fr, int fq) const {
;     ...
;         for (int ai = 0; ai < 2; ++ai)
; #pragma unroll
;             for (int m = 0; m < 4; ++m) { const size_t row = (size_t)(row0 + ai * 128 + m * 16);
; #pragma unroll
;                 for (int bj = 0; bj < 2; ++bj) { const int col = col0 + bj * 128; const v2u ga = *(const v2u*)(GATES + row * 4096 + col), gs = *(const v2u*)(GATES + row * 4096 + 2048 + col);
;                     f32x4& a0 = acc[ai][bj][m][0]; f32x4& a1 = acc[ai][bj][m][1];
; #pragma unroll
;                     for (int e = 0; e < 4; ++e) { a0[e] *= (float)((ga.x >> (8 * e)) & 0xffu) * __builtin_amdgcn_rcpf((float)((gs.x >> (8 * e)) & 0xffu));
;                                                   a1[e] *= (float)((ga.y >> (8 * e)) & 0xffu) * __builtin_amdgcn_rcpf((float)((gs.y >> (8 * e)) & 0xffu)); } } }
	v_cvt_f32_ubyte0_e32 v232, v195
	v_cvt_f32_ubyte1_e32 v233, v195
	v_rcp_iflag_f32_e32 v232, v232
	v_rcp_iflag_f32_e32 v233, v233
	v_cvt_f32_ubyte0_e32 v234, v191
	v_cvt_f32_ubyte1_e32 v235, v191
	v_pk_mul_f32 v[232:233], v[232:233], v[234:235]
	v_pk_mul_f32 v[94:95], v[94:95], v[232:233]
	v_cvt_f32_ubyte2_e32 v236, v195
	v_cvt_f32_ubyte3_e32 v237, v195
	v_rcp_iflag_f32_e32 v236, v236
	v_rcp_iflag_f32_e32 v237, v237
	v_cvt_f32_ubyte2_e32 v238, v191
	v_cvt_f32_ubyte3_e32 v239, v191
	v_pk_mul_f32 v[236:237], v[236:237], v[238:239]
	v_pk_mul_f32 v[96:97], v[96:97], v[236:237]
	v_cvt_f32_ubyte0_e32 v232, v194
	v_cvt_f32_ubyte1_e32 v233, v194
	v_rcp_iflag_f32_e32 v232, v232
	v_rcp_iflag_f32_e32 v233, v233
	v_cvt_f32_ubyte0_e32 v234, v190
	v_cvt_f32_ubyte1_e32 v235, v190
	v_pk_mul_f32 v[232:233], v[232:233], v[234:235]
	v_pk_mul_f32 v[98:99], v[98:99], v[232:233]
	v_cvt_f32_ubyte2_e32 v236, v194
	v_cvt_f32_ubyte3_e32 v237, v194
	v_rcp_iflag_f32_e32 v236, v236
	v_rcp_iflag_f32_e32 v237, v237
	v_cvt_f32_ubyte2_e32 v238, v190
	v_cvt_f32_ubyte3_e32 v239, v190
	v_pk_mul_f32 v[236:237], v[236:237], v[238:239]
	v_pk_mul_f32 v[100:101], v[100:101], v[236:237]
	v_cvt_f32_ubyte0_e32 v232, v193
	v_cvt_f32_ubyte1_e32 v233, v193
	v_rcp_iflag_f32_e32 v232, v232
	v_rcp_iflag_f32_e32 v233, v233
	v_cvt_f32_ubyte0_e32 v234, v185
	v_cvt_f32_ubyte1_e32 v235, v185
	v_pk_mul_f32 v[232:233], v[232:233], v[234:235]
	v_pk_mul_f32 v[102:103], v[102:103], v[232:233]
	v_cvt_f32_ubyte2_e32 v236, v193
	v_cvt_f32_ubyte3_e32 v237, v193
	v_rcp_iflag_f32_e32 v236, v236
	v_rcp_iflag_f32_e32 v237, v237
	v_cvt_f32_ubyte2_e32 v238, v185
	v_cvt_f32_ubyte3_e32 v239, v185
	v_pk_mul_f32 v[236:237], v[236:237], v[238:239]
	v_pk_mul_f32 v[104:105], v[104:105], v[236:237]
	v_cvt_f32_ubyte0_e32 v232, v192
	v_cvt_f32_ubyte1_e32 v233, v192
	v_rcp_iflag_f32_e32 v232, v232
	v_rcp_iflag_f32_e32 v233, v233
	v_cvt_f32_ubyte0_e32 v234, v184
	v_cvt_f32_ubyte1_e32 v235, v184
	v_pk_mul_f32 v[232:233], v[232:233], v[234:235]
	v_pk_mul_f32 v[106:107], v[106:107], v[232:233]
	v_cvt_f32_ubyte2_e32 v236, v192
	v_cvt_f32_ubyte3_e32 v237, v192
	v_rcp_iflag_f32_e32 v236, v236
	v_rcp_iflag_f32_e32 v237, v237
	v_cvt_f32_ubyte2_e32 v238, v184
	v_cvt_f32_ubyte3_e32 v239, v184
	v_pk_mul_f32 v[236:237], v[236:237], v[238:239]
	v_pk_mul_f32 v[108:109], v[108:109], v[236:237]
	s_waitcnt vmcnt(12)
	v_cvt_f32_ubyte0_e32 v232, v203
	v_cvt_f32_ubyte1_e32 v233, v203
	v_rcp_iflag_f32_e32 v232, v232
	v_rcp_iflag_f32_e32 v233, v233
	v_cvt_f32_ubyte0_e32 v234, v199
	v_cvt_f32_ubyte1_e32 v235, v199
	v_pk_mul_f32 v[232:233], v[232:233], v[234:235]
	v_pk_mul_f32 v[78:79], v[78:79], v[232:233]
	v_cvt_f32_ubyte2_e32 v236, v203
	v_cvt_f32_ubyte3_e32 v237, v203
	v_rcp_iflag_f32_e32 v236, v236
	v_rcp_iflag_f32_e32 v237, v237
	v_cvt_f32_ubyte2_e32 v238, v199
	v_cvt_f32_ubyte3_e32 v239, v199
	v_pk_mul_f32 v[236:237], v[236:237], v[238:239]
	v_pk_mul_f32 v[80:81], v[80:81], v[236:237]
	v_cvt_f32_ubyte0_e32 v232, v202
	v_cvt_f32_ubyte1_e32 v233, v202
	v_rcp_iflag_f32_e32 v232, v232
	v_rcp_iflag_f32_e32 v233, v233
	v_cvt_f32_ubyte0_e32 v234, v198
	v_cvt_f32_ubyte1_e32 v235, v198
	v_pk_mul_f32 v[232:233], v[232:233], v[234:235]
	v_pk_mul_f32 v[82:83], v[82:83], v[232:233]
	v_cvt_f32_ubyte2_e32 v236, v202
	v_cvt_f32_ubyte3_e32 v237, v202
	v_rcp_iflag_f32_e32 v236, v236
	v_rcp_iflag_f32_e32 v237, v237
	v_cvt_f32_ubyte2_e32 v238, v198
	v_cvt_f32_ubyte3_e32 v239, v198
	v_pk_mul_f32 v[236:237], v[236:237], v[238:239]
	v_pk_mul_f32 v[84:85], v[84:85], v[236:237]
	v_cvt_f32_ubyte0_e32 v232, v201
	v_cvt_f32_ubyte1_e32 v233, v201
	v_rcp_iflag_f32_e32 v232, v232
	v_rcp_iflag_f32_e32 v233, v233
	v_cvt_f32_ubyte0_e32 v234, v197
	v_cvt_f32_ubyte1_e32 v235, v197
	v_pk_mul_f32 v[232:233], v[232:233], v[234:235]
	v_pk_mul_f32 v[86:87], v[86:87], v[232:233]
	v_cvt_f32_ubyte2_e32 v236, v201
	v_cvt_f32_ubyte3_e32 v237, v201
	v_rcp_iflag_f32_e32 v236, v236
	v_rcp_iflag_f32_e32 v237, v237
	v_cvt_f32_ubyte2_e32 v238, v197
	v_cvt_f32_ubyte3_e32 v239, v197
	v_pk_mul_f32 v[236:237], v[236:237], v[238:239]
	v_pk_mul_f32 v[88:89], v[88:89], v[236:237]
	v_cvt_f32_ubyte0_e32 v232, v200
	v_cvt_f32_ubyte1_e32 v233, v200
	v_rcp_iflag_f32_e32 v232, v232
	v_rcp_iflag_f32_e32 v233, v233
	v_cvt_f32_ubyte0_e32 v234, v196
	v_cvt_f32_ubyte1_e32 v235, v196
	v_pk_mul_f32 v[232:233], v[232:233], v[234:235]
	v_pk_mul_f32 v[90:91], v[90:91], v[232:233]
	v_cvt_f32_ubyte2_e32 v236, v200
	v_cvt_f32_ubyte3_e32 v237, v200
	v_rcp_iflag_f32_e32 v236, v236
	v_rcp_iflag_f32_e32 v237, v237
	v_cvt_f32_ubyte2_e32 v238, v196
	v_cvt_f32_ubyte3_e32 v239, v196
	v_pk_mul_f32 v[236:237], v[236:237], v[238:239]
	v_pk_mul_f32 v[92:93], v[92:93], v[236:237]
	s_waitcnt vmcnt(8)
;     __device__ __forceinline__ void mid(f32x4 (&acc)[2][2][4][2], const Unit& u, int wr, int wc, int fr, int fq) const {
;     ...
;         for (int ai = 0; ai < 2; ++ai)
; #pragma unroll
;             for (int m = 0; m < 4; ++m) { const size_t row = (size_t)(row0 + ai * 128 + m * 16);
; #pragma unroll
;                 for (int bj = 0; bj < 2; ++bj) { const int col = col0 + bj * 128; const v2u ga = *(const v2u*)(GATES + row * 4096 + col), gs = *(const v2u*)(GATES + row * 4096 + 2048 + col);
;                     f32x4& a0 = acc[ai][bj][m][0]; f32x4& a1 = acc[ai][bj][m][1];
; #pragma unroll
;                     for (int e = 0; e < 4; ++e) { a0[e] *= (float)((ga.x >> (8 * e)) & 0xffu) * __builtin_amdgcn_rcpf((float)((gs.x >> (8 * e)) & 0xffu));
;                                                   a1[e] *= (float)((ga.y >> (8 * e)) & 0xffu) * __builtin_amdgcn_rcpf((float)((gs.y >> (8 * e)) & 0xffu)); } } }
	v_cvt_f32_ubyte0_e32 v232, v211
	v_cvt_f32_ubyte1_e32 v233, v211
	v_rcp_iflag_f32_e32 v232, v232
	v_rcp_iflag_f32_e32 v233, v233
	v_cvt_f32_ubyte0_e32 v234, v207
	v_cvt_f32_ubyte1_e32 v235, v207
	v_pk_mul_f32 v[232:233], v[232:233], v[234:235]
	v_pk_mul_f32 v[62:63], v[62:63], v[232:233]
	v_cvt_f32_ubyte2_e32 v236, v211
	v_cvt_f32_ubyte3_e32 v237, v211
	v_rcp_iflag_f32_e32 v236, v236
	v_rcp_iflag_f32_e32 v237, v237
	v_cvt_f32_ubyte2_e32 v238, v207
	v_cvt_f32_ubyte3_e32 v239, v207
	v_pk_mul_f32 v[236:237], v[236:237], v[238:239]
	v_pk_mul_f32 v[64:65], v[64:65], v[236:237]
	v_cvt_f32_ubyte0_e32 v232, v210
	v_cvt_f32_ubyte1_e32 v233, v210
	v_rcp_iflag_f32_e32 v232, v232
	v_rcp_iflag_f32_e32 v233, v233
	v_cvt_f32_ubyte0_e32 v234, v206
	v_cvt_f32_ubyte1_e32 v235, v206
	v_pk_mul_f32 v[232:233], v[232:233], v[234:235]
	v_pk_mul_f32 v[66:67], v[66:67], v[232:233]
	v_cvt_f32_ubyte2_e32 v236, v210
	v_cvt_f32_ubyte3_e32 v237, v210
	v_rcp_iflag_f32_e32 v236, v236
	v_rcp_iflag_f32_e32 v237, v237
	v_cvt_f32_ubyte2_e32 v238, v206
	v_cvt_f32_ubyte3_e32 v239, v206
	v_pk_mul_f32 v[236:237], v[236:237], v[238:239]
	v_pk_mul_f32 v[68:69], v[68:69], v[236:237]
	v_cvt_f32_ubyte0_e32 v232, v209
	v_cvt_f32_ubyte1_e32 v233, v209
	v_rcp_iflag_f32_e32 v232, v232
	v_rcp_iflag_f32_e32 v233, v233
	v_cvt_f32_ubyte0_e32 v234, v205
	v_cvt_f32_ubyte1_e32 v235, v205
	v_pk_mul_f32 v[232:233], v[232:233], v[234:235]
	v_pk_mul_f32 v[70:71], v[70:71], v[232:233]
	v_cvt_f32_ubyte2_e32 v236, v209
	v_cvt_f32_ubyte3_e32 v237, v209
	v_rcp_iflag_f32_e32 v236, v236
	v_rcp_iflag_f32_e32 v237, v237
	v_cvt_f32_ubyte2_e32 v238, v205
	v_cvt_f32_ubyte3_e32 v239, v205
	v_pk_mul_f32 v[236:237], v[236:237], v[238:239]
	v_pk_mul_f32 v[72:73], v[72:73], v[236:237]
	v_cvt_f32_ubyte0_e32 v232, v208
	v_cvt_f32_ubyte1_e32 v233, v208
	v_rcp_iflag_f32_e32 v232, v232
	v_rcp_iflag_f32_e32 v233, v233
	v_cvt_f32_ubyte0_e32 v234, v204
	v_cvt_f32_ubyte1_e32 v235, v204
	v_pk_mul_f32 v[232:233], v[232:233], v[234:235]
	v_pk_mul_f32 v[74:75], v[74:75], v[232:233]
	v_cvt_f32_ubyte2_e32 v236, v208
	v_cvt_f32_ubyte3_e32 v237, v208
	v_rcp_iflag_f32_e32 v236, v236
	v_rcp_iflag_f32_e32 v237, v237
	v_cvt_f32_ubyte2_e32 v238, v204
	v_cvt_f32_ubyte3_e32 v239, v204
	v_pk_mul_f32 v[236:237], v[236:237], v[238:239]
	v_pk_mul_f32 v[76:77], v[76:77], v[236:237]
	s_waitcnt vmcnt(4)
	v_cvt_f32_ubyte0_e32 v232, v219
	v_cvt_f32_ubyte1_e32 v233, v219
	v_rcp_iflag_f32_e32 v232, v232
	v_rcp_iflag_f32_e32 v233, v233
	v_cvt_f32_ubyte0_e32 v234, v215
	v_cvt_f32_ubyte1_e32 v235, v215
	v_pk_mul_f32 v[232:233], v[232:233], v[234:235]
	v_pk_mul_f32 v[46:47], v[46:47], v[232:233]
	v_cvt_f32_ubyte2_e32 v236, v219
	v_cvt_f32_ubyte3_e32 v237, v219
	v_rcp_iflag_f32_e32 v236, v236
	v_rcp_iflag_f32_e32 v237, v237
	v_cvt_f32_ubyte2_e32 v238, v215
	v_cvt_f32_ubyte3_e32 v239, v215
	v_pk_mul_f32 v[236:237], v[236:237], v[238:239]
	v_pk_mul_f32 v[48:49], v[48:49], v[236:237]
	v_cvt_f32_ubyte0_e32 v232, v218
	v_cvt_f32_ubyte1_e32 v233, v218
	v_rcp_iflag_f32_e32 v232, v232
	v_rcp_iflag_f32_e32 v233, v233
	v_cvt_f32_ubyte0_e32 v234, v214
	v_cvt_f32_ubyte1_e32 v235, v214
	v_pk_mul_f32 v[232:233], v[232:233], v[234:235]
	v_pk_mul_f32 v[50:51], v[50:51], v[232:233]
	v_cvt_f32_ubyte2_e32 v236, v218
	v_cvt_f32_ubyte3_e32 v237, v218
	v_rcp_iflag_f32_e32 v236, v236
	v_rcp_iflag_f32_e32 v237, v237
	v_cvt_f32_ubyte2_e32 v238, v214
	v_cvt_f32_ubyte3_e32 v239, v214
	v_pk_mul_f32 v[236:237], v[236:237], v[238:239]
	v_pk_mul_f32 v[52:53], v[52:53], v[236:237]
	v_cvt_f32_ubyte0_e32 v232, v217
	v_cvt_f32_ubyte1_e32 v233, v217
	v_rcp_iflag_f32_e32 v232, v232
	v_rcp_iflag_f32_e32 v233, v233
	v_cvt_f32_ubyte0_e32 v234, v213
	v_cvt_f32_ubyte1_e32 v235, v213
	v_pk_mul_f32 v[232:233], v[232:233], v[234:235]
	v_pk_mul_f32 v[54:55], v[54:55], v[232:233]
	v_cvt_f32_ubyte2_e32 v236, v217
	v_cvt_f32_ubyte3_e32 v237, v217
	v_rcp_iflag_f32_e32 v236, v236
	v_rcp_iflag_f32_e32 v237, v237
	v_cvt_f32_ubyte2_e32 v238, v213
	v_cvt_f32_ubyte3_e32 v239, v213
	v_pk_mul_f32 v[236:237], v[236:237], v[238:239]
	v_pk_mul_f32 v[56:57], v[56:57], v[236:237]
	v_cvt_f32_ubyte0_e32 v232, v216
	v_cvt_f32_ubyte1_e32 v233, v216
	v_rcp_iflag_f32_e32 v232, v232
	v_rcp_iflag_f32_e32 v233, v233
	v_cvt_f32_ubyte0_e32 v234, v212
	v_cvt_f32_ubyte1_e32 v235, v212
	v_pk_mul_f32 v[232:233], v[232:233], v[234:235]
	v_pk_mul_f32 v[58:59], v[58:59], v[232:233]
	v_cvt_f32_ubyte2_e32 v236, v216
	v_cvt_f32_ubyte3_e32 v237, v216
	v_rcp_iflag_f32_e32 v236, v236
	v_rcp_iflag_f32_e32 v237, v237
	v_cvt_f32_ubyte2_e32 v238, v212
	v_cvt_f32_ubyte3_e32 v239, v212
	v_pk_mul_f32 v[236:237], v[236:237], v[238:239]
	v_pk_mul_f32 v[60:61], v[60:61], v[236:237]
	s_waitcnt vmcnt(0)
	v_cvt_f32_ubyte0_e32 v232, v227
	v_cvt_f32_ubyte1_e32 v233, v227
	v_rcp_iflag_f32_e32 v232, v232
	v_rcp_iflag_f32_e32 v233, v233
	v_cvt_f32_ubyte0_e32 v234, v223
	v_cvt_f32_ubyte1_e32 v235, v223
	v_pk_mul_f32 v[232:233], v[232:233], v[234:235]
	v_pk_mul_f32 v[30:31], v[30:31], v[232:233]
	v_cvt_f32_ubyte2_e32 v236, v227
	v_cvt_f32_ubyte3_e32 v237, v227
	v_rcp_iflag_f32_e32 v236, v236
	v_rcp_iflag_f32_e32 v237, v237
	v_cvt_f32_ubyte2_e32 v238, v223
	v_cvt_f32_ubyte3_e32 v239, v223
	v_pk_mul_f32 v[236:237], v[236:237], v[238:239]
	v_pk_mul_f32 v[32:33], v[32:33], v[236:237]
	v_cvt_f32_ubyte0_e32 v232, v226
	v_cvt_f32_ubyte1_e32 v233, v226
	v_rcp_iflag_f32_e32 v232, v232
	v_rcp_iflag_f32_e32 v233, v233
	v_cvt_f32_ubyte0_e32 v234, v222
	v_cvt_f32_ubyte1_e32 v235, v222
	v_pk_mul_f32 v[232:233], v[232:233], v[234:235]
	v_pk_mul_f32 v[34:35], v[34:35], v[232:233]
	v_cvt_f32_ubyte2_e32 v236, v226
	v_cvt_f32_ubyte3_e32 v237, v226
	v_rcp_iflag_f32_e32 v236, v236
	v_rcp_iflag_f32_e32 v237, v237
	v_cvt_f32_ubyte2_e32 v238, v222
	v_cvt_f32_ubyte3_e32 v239, v222
	v_pk_mul_f32 v[236:237], v[236:237], v[238:239]
	v_pk_mul_f32 v[36:37], v[36:37], v[236:237]
	v_cvt_f32_ubyte0_e32 v232, v225
	v_cvt_f32_ubyte1_e32 v233, v225
	v_rcp_iflag_f32_e32 v232, v232
	v_rcp_iflag_f32_e32 v233, v233
	v_cvt_f32_ubyte0_e32 v234, v221
	v_cvt_f32_ubyte1_e32 v235, v221
	v_pk_mul_f32 v[232:233], v[232:233], v[234:235]
	v_pk_mul_f32 v[38:39], v[38:39], v[232:233]
	v_cvt_f32_ubyte2_e32 v236, v225
	v_cvt_f32_ubyte3_e32 v237, v225
	v_rcp_iflag_f32_e32 v236, v236
	v_rcp_iflag_f32_e32 v237, v237
	v_cvt_f32_ubyte2_e32 v238, v221
	v_cvt_f32_ubyte3_e32 v239, v221
	v_pk_mul_f32 v[236:237], v[236:237], v[238:239]
	v_pk_mul_f32 v[40:41], v[40:41], v[236:237]
	v_cvt_f32_ubyte0_e32 v232, v224
	v_cvt_f32_ubyte1_e32 v233, v224
	v_rcp_iflag_f32_e32 v232, v232
	v_rcp_iflag_f32_e32 v233, v233
	v_cvt_f32_ubyte0_e32 v234, v220
	v_cvt_f32_ubyte1_e32 v235, v220
	v_pk_mul_f32 v[232:233], v[232:233], v[234:235]
	v_pk_mul_f32 v[42:43], v[42:43], v[232:233]
	v_cvt_f32_ubyte2_e32 v236, v224
	v_cvt_f32_ubyte3_e32 v237, v224
	v_rcp_iflag_f32_e32 v236, v236
	v_rcp_iflag_f32_e32 v237, v237
	v_cvt_f32_ubyte2_e32 v238, v220
	v_cvt_f32_ubyte3_e32 v239, v220
	v_pk_mul_f32 v[236:237], v[236:237], v[238:239]
	v_pk_mul_f32 v[44:45], v[44:45], v[236:237]
	s_branch .LBB0_954
